# grid barrier: all workgroups poll the top counter directly (no per-XCD generation hop); MLA loop: row-sum adds unpacked, 8 K-fragment LDS reads per half hoisted into free registers
# speedup vs baseline: 1.0264x; 1.0017x over previous
.LBB0_347:
	s_or_b64 exec, exec, s[4:5]
	v_cvt_f32_u32_e32 v6, v4
	s_waitcnt vmcnt(0)
	v_readfirstlane_b32 s4, v5
	v_sub_u32_e32 v5, 0, v4
	v_rcp_iflag_f32_e32 v6, v6
	v_add_u32_e32 v7, s4, v1
	v_mul_f32_e32 v6, 0x4f7ffffe, v6
	v_cvt_u32_f32_e32 v6, v6
	v_mul_lo_u32 v1, v5, v6
	v_mul_hi_u32 v1, v6, v1
	v_add_u32_e32 v1, v6, v1
	v_mul_hi_u32 v1, v7, v1
	v_mul_lo_u32 v5, v1, v4
	v_sub_u32_e32 v5, v7, v5
	v_add_u32_e32 v6, 1, v1
	v_cmp_ge_u32_e32 vcc, v5, v4
	s_nop 1
	v_cndmask_b32_e32 v1, v1, v6, vcc
	v_sub_u32_e32 v6, v5, v4
	v_cndmask_b32_e32 v5, v5, v6, vcc
	v_add_u32_e32 v6, 1, v1
	v_cmp_ge_u32_e32 vcc, v5, v4
	v_add_u32_e32 v5, 1, v7
	s_nop 0
	v_cndmask_b32_e32 v1, v1, v6, vcc
	v_mul_lo_u32 v6, v4, v1
	v_add_u32_e32 v4, v6, v4
	v_cmp_ne_u32_e32 vcc, v5, v4
	s_and_saveexec_b64 s[4:5], vcc
	s_xor_b64 s[4:5], exec, s[4:5]
	s_cbranch_execz .LBB0_361
	v_readlane_b32 s10, v250, 62
	v_readlane_b32 s11, v250, 63
	s_waitcnt lgkmcnt(0)
	v_add_u32_e32 v1, 1, v1
	v_mul_lo_u32 v1, v1, v2
	s_nop 3
	global_load_dword v2, v3, s[10:11] sc1
	s_waitcnt vmcnt(0)
	v_cmp_lt_u32_e32 vcc, v2, v1
	s_and_saveexec_b64 s[36:37], vcc
	s_cbranch_execz .LBB0_360
	s_mov_b32 s12, 1
	s_mov_b64 s[38:39], 0
	s_branch .LBB0_351

.LBB0_353:
	v_readlane_b32 s10, v250, 62
	v_readlane_b32 s11, v250, 63
	s_add_i32 s12, s12, 1
	s_mov_b64 s[42:43], -1
	s_nop 2
	global_load_dword v2, v3, s[10:11] sc1
	s_waitcnt vmcnt(0)
	v_cmp_ge_u32_e32 vcc, v2, v1
	s_orn2_b64 s[10:11], vcc, exec
	s_branch .LBB0_350

.LBB0_364:
	s_or_b64 exec, exec, s[10:11]
	s_waitcnt vmcnt(0)
	v_readfirstlane_b32 s4, v4
	v_sub_u32_e32 v5, 0, v2
	s_mov_b64 s[10:11], 0
	v_add_u32_e32 v4, s4, v1
	v_cvt_f32_u32_e32 v1, v2
	v_readlane_b32 s4, v251, 0
	v_readlane_b32 s5, v251, 1
	v_rcp_iflag_f32_e32 v1, v1
	s_nop 0
	v_mul_f32_e32 v1, 0x4f7ffffe, v1
	v_cvt_u32_f32_e32 v1, v1
	v_mul_lo_u32 v5, v5, v1
	v_mul_hi_u32 v5, v1, v5
	v_add_u32_e32 v1, v1, v5
	v_mul_hi_u32 v1, v4, v1
	v_mul_lo_u32 v5, v1, v2
	v_sub_u32_e32 v5, v4, v5
	v_cmp_ge_u32_e32 vcc, v5, v2
	v_add_u32_e32 v6, 1, v1
	v_add_u32_e32 v4, 1, v4
	v_cndmask_b32_e32 v1, v1, v6, vcc
	v_sub_u32_e32 v6, v5, v2
	v_cndmask_b32_e32 v5, v5, v6, vcc
	v_cmp_ge_u32_e32 vcc, v5, v2
	v_add_u32_e32 v5, 1, v1
	s_nop 0
	v_cndmask_b32_e32 v1, v1, v5, vcc
	v_mul_lo_u32 v5, v2, v1
	v_add_u32_e32 v2, v5, v2
	v_cmp_ne_u32_e32 vcc, v4, v2
	v_mov_b32_e32 v1, v2
	v_mov_b64_e32 v[4:5], s[4:5]
	s_and_saveexec_b64 s[4:5], vcc
	s_cbranch_execz .LBB0_376
	v_readlane_b32 s10, v250, 62
	v_readlane_b32 s11, v250, 63
	s_nop 4
	global_load_dword v2, v3, s[10:11] sc1
	s_mov_b64 s[10:11], 0
	s_waitcnt vmcnt(0)
	v_cmp_lt_u32_e32 vcc, v2, v1
	s_and_saveexec_b64 s[36:37], vcc
	s_cbranch_execz .LBB0_375
	s_mov_b32 s12, 1
	s_mov_b64 s[38:39], 0
	s_branch .LBB0_368

.LBB0_378:
	s_or_b64 exec, exec, s[4:5]
	s_mov_b64 s[4:5], exec
	v_mbcnt_lo_u32_b32 v1, s4, 0
	v_mbcnt_hi_u32_b32 v1, s5, v1
	v_cmp_eq_u32_e32 vcc, 0, v1
	s_waitcnt vmcnt(0)
	buffer_inv sc1
	s_and_saveexec_b64 s[10:11], vcc
	s_cbranch_execz .LBB0_380
	s_bcnt1_i32_b64 s4, s[4:5]
	v_mov_b32_e32 v1, s4
	v_readlane_b32 s4, v250, 60
	v_readlane_b32 s5, v250, 61
	s_nop 4
.LBB0_380:
	s_or_b64 exec, exec, s[10:11]
	s_waitcnt vmcnt(0)

.LBB0_424:
	s_or_b64 exec, exec, s[4:5]
	v_cvt_f32_u32_e32 v6, v4
	s_waitcnt vmcnt(0)
	v_readfirstlane_b32 s4, v5
	v_sub_u32_e32 v5, 0, v4
	v_rcp_iflag_f32_e32 v6, v6
	v_add_u32_e32 v7, s4, v1
	v_mul_f32_e32 v6, 0x4f7ffffe, v6
	v_cvt_u32_f32_e32 v6, v6
	v_mul_lo_u32 v1, v5, v6
	v_mul_hi_u32 v1, v6, v1
	v_add_u32_e32 v1, v6, v1
	v_mul_hi_u32 v1, v7, v1
	v_mul_lo_u32 v5, v1, v4
	v_sub_u32_e32 v5, v7, v5
	v_add_u32_e32 v6, 1, v1
	v_cmp_ge_u32_e32 vcc, v5, v4
	s_nop 1
	v_cndmask_b32_e32 v1, v1, v6, vcc
	v_sub_u32_e32 v6, v5, v4
	v_cndmask_b32_e32 v5, v5, v6, vcc
	v_add_u32_e32 v6, 1, v1
	v_cmp_ge_u32_e32 vcc, v5, v4
	v_add_u32_e32 v5, 1, v7
	s_nop 0
	v_cndmask_b32_e32 v1, v1, v6, vcc
	v_mul_lo_u32 v6, v4, v1
	v_add_u32_e32 v4, v6, v4
	v_cmp_ne_u32_e32 vcc, v5, v4
	s_and_saveexec_b64 s[4:5], vcc
	s_xor_b64 s[4:5], exec, s[4:5]
	s_cbranch_execz .LBB0_438
	v_readlane_b32 s10, v250, 62
	v_readlane_b32 s11, v250, 63
	s_waitcnt lgkmcnt(0)
	v_add_u32_e32 v1, 1, v1
	v_mul_lo_u32 v1, v1, v2
	s_nop 3
	global_load_dword v2, v3, s[10:11] sc1
	s_waitcnt vmcnt(0)
	v_cmp_lt_u32_e32 vcc, v2, v1
	s_and_saveexec_b64 s[36:37], vcc
	s_cbranch_execz .LBB0_437
	s_mov_b32 s46, 1
	s_mov_b64 s[38:39], 0
	s_branch .LBB0_428

.LBB0_430:
	v_readlane_b32 s10, v250, 62
	v_readlane_b32 s11, v250, 63
	s_add_i32 s46, s46, 1
	s_mov_b64 s[42:43], -1
	s_nop 2
	global_load_dword v2, v3, s[10:11] sc1
	s_waitcnt vmcnt(0)
	v_cmp_ge_u32_e32 vcc, v2, v1
	s_orn2_b64 s[10:11], vcc, exec
	s_branch .LBB0_427

.LBB0_441:
	s_or_b64 exec, exec, s[10:11]
	s_waitcnt vmcnt(0)
	v_readfirstlane_b32 s4, v4
	v_sub_u32_e32 v5, 0, v2
	s_mov_b64 s[10:11], 0
	v_add_u32_e32 v4, s4, v1
	v_cvt_f32_u32_e32 v1, v2
	v_readlane_b32 s4, v251, 0
	v_readlane_b32 s5, v251, 1
	v_rcp_iflag_f32_e32 v1, v1
	s_nop 0
	v_mul_f32_e32 v1, 0x4f7ffffe, v1
	v_cvt_u32_f32_e32 v1, v1
	v_mul_lo_u32 v5, v5, v1
	v_mul_hi_u32 v5, v1, v5
	v_add_u32_e32 v1, v1, v5
	v_mul_hi_u32 v1, v4, v1
	v_mul_lo_u32 v5, v1, v2
	v_sub_u32_e32 v5, v4, v5
	v_cmp_ge_u32_e32 vcc, v5, v2
	v_add_u32_e32 v6, 1, v1
	v_add_u32_e32 v4, 1, v4
	v_cndmask_b32_e32 v1, v1, v6, vcc
	v_sub_u32_e32 v6, v5, v2
	v_cndmask_b32_e32 v5, v5, v6, vcc
	v_cmp_ge_u32_e32 vcc, v5, v2
	v_add_u32_e32 v5, 1, v1
	s_nop 0
	v_cndmask_b32_e32 v1, v1, v5, vcc
	v_mul_lo_u32 v5, v2, v1
	v_add_u32_e32 v2, v5, v2
	v_cmp_ne_u32_e32 vcc, v4, v2
	v_mov_b32_e32 v1, v2
	v_mov_b64_e32 v[4:5], s[4:5]
	s_and_saveexec_b64 s[4:5], vcc
	s_cbranch_execz .LBB0_453
	v_readlane_b32 s10, v250, 62
	v_readlane_b32 s11, v250, 63
	s_nop 4
	global_load_dword v2, v3, s[10:11] sc1
	s_mov_b64 s[10:11], 0
	s_waitcnt vmcnt(0)
	v_cmp_lt_u32_e32 vcc, v2, v1
	s_and_saveexec_b64 s[36:37], vcc
	s_cbranch_execz .LBB0_452
	s_mov_b32 s46, 1
	s_mov_b64 s[38:39], 0
	s_branch .LBB0_445

.LBB0_455:
	s_or_b64 exec, exec, s[4:5]
	s_mov_b64 s[4:5], exec
	v_mbcnt_lo_u32_b32 v1, s4, 0
	v_mbcnt_hi_u32_b32 v1, s5, v1
	v_cmp_eq_u32_e32 vcc, 0, v1
	s_waitcnt vmcnt(0)
	buffer_inv sc1
	s_and_saveexec_b64 s[10:11], vcc
	s_cbranch_execz .LBB0_457
	s_bcnt1_i32_b64 s4, s[4:5]
	v_mov_b32_e32 v1, s4
	v_readlane_b32 s4, v250, 60
	v_readlane_b32 s5, v250, 61
	s_nop 4
.LBB0_457:
	s_or_b64 exec, exec, s[10:11]
	s_waitcnt vmcnt(0)

.LBB0_534:
	s_or_b64 exec, exec, s[4:5]
	v_cvt_f32_u32_e32 v6, v4
	s_waitcnt vmcnt(0)
	v_readfirstlane_b32 s4, v5
	v_sub_u32_e32 v5, 0, v4
	v_rcp_iflag_f32_e32 v6, v6
	v_add_u32_e32 v7, s4, v1
	v_mul_f32_e32 v6, 0x4f7ffffe, v6
	v_cvt_u32_f32_e32 v6, v6
	v_mul_lo_u32 v1, v5, v6
	v_mul_hi_u32 v1, v6, v1
	v_add_u32_e32 v1, v6, v1
	v_mul_hi_u32 v1, v7, v1
	v_mul_lo_u32 v5, v1, v4
	v_sub_u32_e32 v5, v7, v5
	v_add_u32_e32 v6, 1, v1
	v_cmp_ge_u32_e32 vcc, v5, v4
	s_nop 1
	v_cndmask_b32_e32 v1, v1, v6, vcc
	v_sub_u32_e32 v6, v5, v4
	v_cndmask_b32_e32 v5, v5, v6, vcc
	v_add_u32_e32 v6, 1, v1
	v_cmp_ge_u32_e32 vcc, v5, v4
	v_add_u32_e32 v5, 1, v7
	s_nop 0
	v_cndmask_b32_e32 v1, v1, v6, vcc
	v_mul_lo_u32 v6, v4, v1
	v_add_u32_e32 v4, v6, v4
	v_cmp_ne_u32_e32 vcc, v5, v4
	s_and_saveexec_b64 s[4:5], vcc
	s_xor_b64 s[4:5], exec, s[4:5]
	s_cbranch_execz .LBB0_548
	v_readlane_b32 s10, v250, 62
	v_readlane_b32 s11, v250, 63
	s_waitcnt lgkmcnt(0)
	v_add_u32_e32 v1, 1, v1
	v_mul_lo_u32 v1, v1, v2
	s_nop 3
	global_load_dword v2, v3, s[10:11] sc1
	s_waitcnt vmcnt(0)
	v_cmp_lt_u32_e32 vcc, v2, v1
	s_and_saveexec_b64 s[38:39], vcc
	s_cbranch_execz .LBB0_547
	s_mov_b32 s48, 1
	s_mov_b64 s[40:41], 0
	s_branch .LBB0_538

.LBB0_540:
	v_readlane_b32 s10, v250, 62
	v_readlane_b32 s11, v250, 63
	s_add_i32 s48, s48, 1
	s_mov_b64 s[44:45], -1
	s_nop 2
	global_load_dword v2, v3, s[10:11] sc1
	s_waitcnt vmcnt(0)
	v_cmp_ge_u32_e32 vcc, v2, v1
	s_orn2_b64 s[10:11], vcc, exec
	s_branch .LBB0_537

.LBB0_551:
	s_or_b64 exec, exec, s[10:11]
	s_waitcnt vmcnt(0)
	v_readfirstlane_b32 s4, v4
	v_sub_u32_e32 v5, 0, v2
	s_mov_b64 s[10:11], 0
	v_add_u32_e32 v4, s4, v1
	v_cvt_f32_u32_e32 v1, v2
	v_readlane_b32 s4, v251, 0
	v_readlane_b32 s5, v251, 1
	v_rcp_iflag_f32_e32 v1, v1
	s_nop 0
	v_mul_f32_e32 v1, 0x4f7ffffe, v1
	v_cvt_u32_f32_e32 v1, v1
	v_mul_lo_u32 v5, v5, v1
	v_mul_hi_u32 v5, v1, v5
	v_add_u32_e32 v1, v1, v5
	v_mul_hi_u32 v1, v4, v1
	v_mul_lo_u32 v5, v1, v2
	v_sub_u32_e32 v5, v4, v5
	v_cmp_ge_u32_e32 vcc, v5, v2
	v_add_u32_e32 v6, 1, v1
	v_add_u32_e32 v4, 1, v4
	v_cndmask_b32_e32 v1, v1, v6, vcc
	v_sub_u32_e32 v6, v5, v2
	v_cndmask_b32_e32 v5, v5, v6, vcc
	v_cmp_ge_u32_e32 vcc, v5, v2
	v_add_u32_e32 v5, 1, v1
	s_nop 0
	v_cndmask_b32_e32 v1, v1, v5, vcc
	v_mul_lo_u32 v5, v2, v1
	v_add_u32_e32 v2, v5, v2
	v_cmp_ne_u32_e32 vcc, v4, v2
	v_mov_b32_e32 v1, v2
	v_mov_b64_e32 v[4:5], s[4:5]
	s_and_saveexec_b64 s[4:5], vcc
	s_cbranch_execz .LBB0_563
	v_readlane_b32 s10, v250, 62
	v_readlane_b32 s11, v250, 63
	s_nop 4
	global_load_dword v2, v3, s[10:11] sc1
	s_mov_b64 s[10:11], 0
	s_waitcnt vmcnt(0)
	v_cmp_lt_u32_e32 vcc, v2, v1
	s_and_saveexec_b64 s[38:39], vcc
	s_cbranch_execz .LBB0_562
	s_mov_b32 s48, 1
	s_mov_b64 s[40:41], 0
	s_branch .LBB0_555

.LBB0_565:
	s_or_b64 exec, exec, s[4:5]
	s_mov_b64 s[4:5], exec
	v_mbcnt_lo_u32_b32 v1, s4, 0
	v_mbcnt_hi_u32_b32 v1, s5, v1
	v_cmp_eq_u32_e32 vcc, 0, v1
	s_waitcnt vmcnt(0)
	buffer_inv sc1
	s_and_saveexec_b64 s[10:11], vcc
	s_cbranch_execz .LBB0_567
	s_bcnt1_i32_b64 s4, s[4:5]
	v_mov_b32_e32 v1, s4
	v_readlane_b32 s4, v250, 60
	v_readlane_b32 s5, v250, 61
	s_nop 4
.LBB0_567:
	s_or_b64 exec, exec, s[10:11]
	s_waitcnt vmcnt(0)

.LBB0_1105:
	s_or_b64 exec, exec, s[4:5]
	v_cvt_f32_u32_e32 v6, v4
	s_waitcnt vmcnt(0)
	v_readfirstlane_b32 s4, v5
	v_sub_u32_e32 v5, 0, v4
	v_rcp_iflag_f32_e32 v6, v6
	v_add_u32_e32 v7, s4, v1
	v_mul_f32_e32 v6, 0x4f7ffffe, v6
	v_cvt_u32_f32_e32 v6, v6
	v_mul_lo_u32 v1, v5, v6
	v_mul_hi_u32 v1, v6, v1
	v_add_u32_e32 v1, v6, v1
	v_mul_hi_u32 v1, v7, v1
	v_mul_lo_u32 v5, v1, v4
	v_sub_u32_e32 v5, v7, v5
	v_add_u32_e32 v6, 1, v1
	v_cmp_ge_u32_e32 vcc, v5, v4
	s_nop 1
	v_cndmask_b32_e32 v1, v1, v6, vcc
	v_sub_u32_e32 v6, v5, v4
	v_cndmask_b32_e32 v5, v5, v6, vcc
	v_add_u32_e32 v6, 1, v1
	v_cmp_ge_u32_e32 vcc, v5, v4
	v_add_u32_e32 v5, 1, v7
	s_nop 0
	v_cndmask_b32_e32 v1, v1, v6, vcc
	v_mul_lo_u32 v6, v4, v1
	v_add_u32_e32 v4, v6, v4
	v_cmp_ne_u32_e32 vcc, v5, v4
	s_and_saveexec_b64 s[4:5], vcc
	s_xor_b64 s[4:5], exec, s[4:5]
	s_cbranch_execz .LBB0_1119
	v_readlane_b32 s10, v250, 62
	v_readlane_b32 s11, v250, 63
	s_waitcnt lgkmcnt(0)
	v_add_u32_e32 v1, 1, v1
	v_mul_lo_u32 v1, v1, v2
	s_nop 3
	global_load_dword v2, v3, s[10:11] sc1
	s_waitcnt vmcnt(0)
	v_cmp_lt_u32_e32 vcc, v2, v1
	s_and_saveexec_b64 s[38:39], vcc
	s_cbranch_execz .LBB0_1118
	s_mov_b32 s42, 1
	s_mov_b64 s[40:41], 0
	s_branch .LBB0_1109

.LBB0_1111:
	v_readlane_b32 s10, v250, 62
	v_readlane_b32 s11, v250, 63
	s_add_i32 s42, s42, 1
	s_mov_b64 s[46:47], -1
	s_nop 2
	global_load_dword v2, v3, s[10:11] sc1
	s_waitcnt vmcnt(0)
	v_cmp_ge_u32_e32 vcc, v2, v1
	s_orn2_b64 s[10:11], vcc, exec
	s_branch .LBB0_1108

.LBB0_1122:
	s_or_b64 exec, exec, s[10:11]
	s_waitcnt vmcnt(0)
	v_readfirstlane_b32 s4, v4
	v_sub_u32_e32 v5, 0, v2
	s_mov_b64 s[10:11], 0
	v_add_u32_e32 v4, s4, v1
	v_cvt_f32_u32_e32 v1, v2
	v_readlane_b32 s4, v251, 0
	v_readlane_b32 s5, v251, 1
	v_rcp_iflag_f32_e32 v1, v1
	s_nop 0
	v_mul_f32_e32 v1, 0x4f7ffffe, v1
	v_cvt_u32_f32_e32 v1, v1
	v_mul_lo_u32 v5, v5, v1
	v_mul_hi_u32 v5, v1, v5
	v_add_u32_e32 v1, v1, v5
	v_mul_hi_u32 v1, v4, v1
	v_mul_lo_u32 v5, v1, v2
	v_sub_u32_e32 v5, v4, v5
	v_cmp_ge_u32_e32 vcc, v5, v2
	v_add_u32_e32 v6, 1, v1
	v_add_u32_e32 v4, 1, v4
	v_cndmask_b32_e32 v1, v1, v6, vcc
	v_sub_u32_e32 v6, v5, v2
	v_cndmask_b32_e32 v5, v5, v6, vcc
	v_cmp_ge_u32_e32 vcc, v5, v2
	v_add_u32_e32 v5, 1, v1
	s_nop 0
	v_cndmask_b32_e32 v1, v1, v5, vcc
	v_mul_lo_u32 v5, v2, v1
	v_add_u32_e32 v2, v5, v2
	v_cmp_ne_u32_e32 vcc, v4, v2
	v_mov_b32_e32 v1, v2
	v_mov_b64_e32 v[4:5], s[4:5]
	s_and_saveexec_b64 s[4:5], vcc
	s_cbranch_execz .LBB0_1134
	v_readlane_b32 s10, v250, 62
	v_readlane_b32 s11, v250, 63
	s_nop 4
	global_load_dword v2, v3, s[10:11] sc1
	s_mov_b64 s[10:11], 0
	s_waitcnt vmcnt(0)
	v_cmp_lt_u32_e32 vcc, v2, v1
	s_and_saveexec_b64 s[38:39], vcc
	s_cbranch_execz .LBB0_1133
	s_mov_b32 s42, 1
	s_mov_b64 s[40:41], 0
	s_branch .LBB0_1126

.LBB0_1136:
	s_or_b64 exec, exec, s[4:5]
	s_mov_b64 s[4:5], exec
	v_mbcnt_lo_u32_b32 v1, s4, 0
	v_mbcnt_hi_u32_b32 v1, s5, v1
	v_cmp_eq_u32_e32 vcc, 0, v1
	s_waitcnt vmcnt(0)
	buffer_inv sc1
	s_and_saveexec_b64 s[10:11], vcc
	s_cbranch_execz .LBB0_1138
	s_bcnt1_i32_b64 s4, s[4:5]
	v_mov_b32_e32 v1, s4
	v_readlane_b32 s4, v250, 60
	v_readlane_b32 s5, v250, 61
	s_nop 4
.LBB0_1138:
	s_or_b64 exec, exec, s[10:11]
	s_waitcnt vmcnt(0)

.LBB0_1236:
	s_or_b64 exec, exec, s[4:5]
	v_pk_add_f32 v[4:5], v[66:67], v[12:13]
	v_add_u32_e32 v2, v2, v161
	v_add_f32_e32 v4, v78, v4
	v_add_f32_e32 v5, v79, v5
	v_add3_u32 v2, v2, v157, v158
	v_add_f32_e32 v4, v16, v4
	v_add_f32_e32 v5, v17, v5
	s_add_i32 s37, s37, 2
	v_add_f32_e32 v4, v52, v4
	v_add_f32_e32 v5, v53, v5
	v_add_u32_e32 v2, 0x3000, v2
	v_add_f32_e32 v4, v14, v4
	v_add_f32_e32 v5, v15, v5
	s_cmp_lt_u32 s38, s12
	v_add_f32_e32 v4, v50, v4
	v_add_f32_e32 v5, v51, v5
	s_waitcnt vmcnt(0)
	ds_write2_b64 v2, v[8:9], v[10:11] offset0:128 offset1:130
	v_add_f32_e32 v4, v68, v4
	v_add_f32_e32 v5, v69, v5
	s_waitcnt lgkmcnt(0)
	v_add_f32_e32 v4, v54, v4
	v_add_f32_e32 v5, v55, v5
	s_barrier
	v_add_f32_e32 v4, v74, v4
	v_add_f32_e32 v5, v75, v5
	s_nop 0
	v_add_f32_e32 v4, v80, v4
	v_add_f32_e32 v5, v81, v5
	s_nop 0
	v_add_f32_e32 v4, v72, v4
	v_add_f32_e32 v5, v73, v5
	s_nop 0
	v_add_f32_e32 v4, v58, v4
	v_add_f32_e32 v5, v59, v5
	s_nop 0
	v_add_f32_e32 v4, v70, v4
	v_add_f32_e32 v5, v71, v5
	s_nop 0
	v_add_f32_e32 v4, v56, v4
	v_add_f32_e32 v5, v57, v5
	s_nop 0
	v_add_f32_e32 v4, v76, v4
	v_add_f32_e32 v5, v77, v5
	s_nop 0
	v_add_f32_e32 v152, v60, v4
	v_add_f32_e32 v153, v61, v5
	s_cbranch_scc0 .LBB0_1331

.LBB0_1246:
	s_or_b64 exec, exec, s[10:11]
	s_add_i32 s5, s39, 1
	s_cmp_lg_u32 s39, 2
	s_cselect_b32 s10, s5, 0
	s_ashr_i32 s5, s4, 31
	v_lshl_add_u64 v[166:167], s[4:5], 1, v[148:149]
	s_mul_i32 s4, s10, 0x5800
	s_add_i32 s40, s4, 0
	v_add3_u32 v12, s40, v159, v160
	ds_read_b128 v[8:11], v12 offset:6656
	v_xor_b32_e32 v66, 0x80000000, v164
	v_mov_b32_e32 v67, v66
	v_mov_b32_e32 v68, v66
	v_mov_b32_e32 v69, v66
	v_mov_b32_e32 v70, v66
	v_mov_b32_e32 v71, v66
	v_mov_b32_e32 v72, v66
	v_mov_b32_e32 v73, v66
	v_mov_b32_e32 v74, v66
	v_mov_b32_e32 v75, v66
	v_mov_b32_e32 v76, v66
	v_mov_b32_e32 v77, v66
	v_mov_b32_e32 v78, v66
	v_mov_b32_e32 v79, v66
	v_mov_b32_e32 v80, v66
	v_mov_b32_e32 v81, v66
	ds_read_b128 v[14:17], v12 offset:6688
	v_max_i32_e32 v13, v82, v98
	s_waitcnt lgkmcnt(1)
	v_mfma_f32_32x32x16_bf16 v[50:65], v[8:11], v[114:117], v[66:81]
	global_load_dwordx4 v[8:11], v[166:167], off
	ds_read_b128 v[166:169], v12
	ds_read_b128 v[170:173], v12 offset:32
	ds_read_b128 v[186:189], v12 offset:64
	ds_read_b128 v[190:193], v12 offset:96
	ds_read_b128 v[194:197], v12 offset:128
	ds_read_b128 v[198:201], v12 offset:160
	ds_read_b128 v[202:205], v12 offset:6720
	ds_read_b128 v[206:209], v12 offset:6752
	ds_read_b128 v[226:229], v12 offset:6784
	ds_read_b128 v[230:233], v12 offset:6816
	v_max3_i32 v13, v13, v83, v99
	v_max3_i32 v13, v13, v84, v100
	v_max3_i32 v13, v13, v85, v101
	v_max3_i32 v13, v13, v86, v102
	v_max3_i32 v13, v13, v87, v103
	s_waitcnt lgkmcnt(9)
	v_mfma_f32_32x32x16_bf16 v[66:81], v[166:169], v[114:117], v[66:81]
	v_max3_i32 v13, v13, v88, v104
	v_max3_i32 v13, v13, v89, v105
	v_max3_i32 v13, v13, v90, v106
	v_max3_i32 v13, v13, v91, v107
	v_max3_i32 v13, v13, v92, v108
	v_max3_i32 v13, v13, v93, v109
	v_max3_i32 v13, v13, v94, v110
	v_mfma_f32_32x32x16_bf16 v[50:65], v[14:17], v[118:121], v[50:65]
	v_max3_i32 v13, v13, v95, v111
	v_max3_i32 v13, v13, v96, v112
	v_max3_i32 v13, v13, v97, v113
	v_mov_b32_e32 v14, v13
	s_nop 1
	v_permlane32_swap_b32_e32 v13, v14
	v_max_i32_e32 v13, v13, v14
	s_waitcnt lgkmcnt(8)
	v_mfma_f32_32x32x16_bf16 v[66:81], v[170:173], v[118:121], v[66:81]
	v_cmp_lt_f32_e32 vcc, s29, v13
	s_cbranch_vccz .LBB0_1248
	v_add_f32_e32 v13, v164, v13
	v_cndmask_b32_e32 v13, v164, v13, vcc
	v_sub_f32_e32 v15, v13, v164
	v_exp_f32_e64 v14, -v15
	v_sub_f32_e32 v97, v97, v15
	v_sub_f32_e32 v96, v96, v15
	v_sub_f32_e32 v95, v95, v15
	v_pk_mul_f32 v[48:49], v[48:49], v[14:15] op_sel_hi:[1,0]
	v_pk_mul_f32 v[46:47], v[46:47], v[14:15] op_sel_hi:[1,0]
	v_pk_mul_f32 v[44:45], v[44:45], v[14:15] op_sel_hi:[1,0]
	v_pk_mul_f32 v[42:43], v[42:43], v[14:15] op_sel_hi:[1,0]
	v_pk_mul_f32 v[40:41], v[40:41], v[14:15] op_sel_hi:[1,0]
	v_pk_mul_f32 v[38:39], v[38:39], v[14:15] op_sel_hi:[1,0]
	v_pk_mul_f32 v[36:37], v[36:37], v[14:15] op_sel_hi:[1,0]
	v_pk_mul_f32 v[34:35], v[34:35], v[14:15] op_sel_hi:[1,0]
	v_pk_mul_f32 v[32:33], v[32:33], v[14:15] op_sel_hi:[1,0]
	v_pk_mul_f32 v[30:31], v[30:31], v[14:15] op_sel_hi:[1,0]
	v_pk_mul_f32 v[28:29], v[28:29], v[14:15] op_sel_hi:[1,0]
	v_pk_mul_f32 v[26:27], v[26:27], v[14:15] op_sel_hi:[1,0]
	v_pk_mul_f32 v[24:25], v[24:25], v[14:15] op_sel_hi:[1,0]
	v_pk_mul_f32 v[22:23], v[22:23], v[14:15] op_sel_hi:[1,0]
	v_pk_mul_f32 v[20:21], v[20:21], v[14:15] op_sel_hi:[1,0]
	v_pk_mul_f32 v[18:19], v[18:19], v[14:15] op_sel_hi:[1,0]
	v_sub_f32_e32 v94, v94, v15
	v_sub_f32_e32 v93, v93, v15
	v_sub_f32_e32 v92, v92, v15
	v_sub_f32_e32 v91, v91, v15
	v_sub_f32_e32 v90, v90, v15
	v_sub_f32_e32 v89, v89, v15
	v_sub_f32_e32 v88, v88, v15
	v_sub_f32_e32 v87, v87, v15
	v_sub_f32_e32 v86, v86, v15
	v_sub_f32_e32 v85, v85, v15
	v_sub_f32_e32 v84, v84, v15
	v_sub_f32_e32 v83, v83, v15
	v_sub_f32_e32 v82, v82, v15
	v_sub_f32_e32 v113, v113, v15
	v_sub_f32_e32 v112, v112, v15
	v_sub_f32_e32 v111, v111, v15
	v_sub_f32_e32 v110, v110, v15
	v_sub_f32_e32 v109, v109, v15
	v_sub_f32_e32 v108, v108, v15
	v_sub_f32_e32 v107, v107, v15
	v_sub_f32_e32 v106, v106, v15
	v_sub_f32_e32 v105, v105, v15
	v_sub_f32_e32 v104, v104, v15
	v_sub_f32_e32 v103, v103, v15
	v_sub_f32_e32 v102, v102, v15
	v_sub_f32_e32 v101, v101, v15
	v_sub_f32_e32 v100, v100, v15
	v_sub_f32_e32 v99, v99, v15
	v_sub_f32_e32 v98, v98, v15
	v_sub_f32_e32 v81, v81, v15
	v_sub_f32_e32 v80, v80, v15
	v_sub_f32_e32 v79, v79, v15
	v_sub_f32_e32 v78, v78, v15
	v_sub_f32_e32 v77, v77, v15
	v_sub_f32_e32 v76, v76, v15
	v_sub_f32_e32 v75, v75, v15
	v_sub_f32_e32 v74, v74, v15
	v_sub_f32_e32 v73, v73, v15
	v_sub_f32_e32 v72, v72, v15
	v_sub_f32_e32 v71, v71, v15
	v_sub_f32_e32 v70, v70, v15
	v_sub_f32_e32 v69, v69, v15
	v_sub_f32_e32 v68, v68, v15
	v_sub_f32_e32 v67, v67, v15
	v_sub_f32_e32 v66, v66, v15
	v_sub_f32_e32 v65, v65, v15
	v_sub_f32_e32 v64, v64, v15
	v_sub_f32_e32 v63, v63, v15
	v_sub_f32_e32 v62, v62, v15
	v_sub_f32_e32 v61, v61, v15
	v_sub_f32_e32 v60, v60, v15
	v_sub_f32_e32 v59, v59, v15
	v_sub_f32_e32 v58, v58, v15
	v_sub_f32_e32 v57, v57, v15
	v_sub_f32_e32 v56, v56, v15
	v_sub_f32_e32 v55, v55, v15
	v_sub_f32_e32 v54, v54, v15
	v_sub_f32_e32 v53, v53, v15
	v_sub_f32_e32 v52, v52, v15
	v_sub_f32_e32 v51, v51, v15
	v_sub_f32_e32 v50, v50, v15
	v_pk_mul_f32 v[152:153], v[152:153], v[14:15] op_sel_hi:[1,0]
	v_mov_b32_e32 v164, v13
.LBB0_1248:
	s_mul_i32 s4, s39, 0x5800
	v_add_u32_e32 v165, s4, v163
	v_exp_f32_e32 v13, v83
	s_waitcnt lgkmcnt(7)
	v_mfma_f32_32x32x16_bf16 v[66:81], v[186:189], v[122:125], v[66:81]
	v_exp_f32_e32 v83, v85
	v_exp_f32_e32 v98, v98
	v_exp_f32_e32 v99, v99
	s_add_i32 s4, s10, 1
	s_cmp_lg_u32 s10, 2
	s_cselect_b32 s39, s4, 0
	s_mul_i32 s41, s39, 0x5800
	s_waitcnt lgkmcnt(6)
	v_mfma_f32_32x32x16_bf16 v[66:81], v[190:193], v[126:129], v[66:81]
	s_add_i32 s42, s41, 0
	s_waitcnt lgkmcnt(5)
	v_mfma_f32_32x32x16_bf16 v[66:81], v[194:197], v[130:133], v[66:81]
	s_waitcnt lgkmcnt(4)
	v_mfma_f32_32x32x16_bf16 v[66:81], v[198:201], v[134:137], v[66:81]
	s_waitcnt lgkmcnt(3)
	v_mfma_f32_32x32x16_bf16 v[50:65], v[202:205], v[122:125], v[50:65]
	s_waitcnt lgkmcnt(2)
	v_mfma_f32_32x32x16_bf16 v[50:65], v[206:209], v[126:129], v[50:65]
	v_exp_f32_e32 v12, v82
	v_exp_f32_e32 v82, v84
	s_waitcnt lgkmcnt(1)
	v_mfma_f32_32x32x16_bf16 v[50:65], v[226:229], v[130:133], v[50:65]
	v_exp_f32_e32 v16, v86
	v_exp_f32_e32 v17, v87
	ds_read_b128 v[84:87], v165 offset:13312
	v_exp_f32_e32 v14, v88
	v_exp_f32_e32 v15, v89
	ds_read_b128 v[170:173], v165 offset:13344
	ds_read_b128 v[178:181], v165 offset:17920
	ds_read_b128 v[182:185], v165 offset:17952
	s_waitcnt lgkmcnt(4)
	v_mfma_f32_32x32x16_bf16 v[50:65], v[230:233], v[134:137], v[50:65]
	v_cvt_pk_bf16_f32 v166, v12, v13
	v_cvt_pk_bf16_f32 v167, v82, v83
	v_cvt_pk_bf16_f32 v168, v16, v17
	v_cvt_pk_bf16_f32 v169, v14, v15
	v_exp_f32_e32 v88, v90
	v_exp_f32_e32 v89, v91
	v_exp_f32_e32 v90, v96
	s_waitcnt lgkmcnt(3)
	v_mfma_f32_32x32x16_bf16 v[34:49], v[84:87], v[166:169], v[34:49]
	v_exp_f32_e32 v86, v92
	v_exp_f32_e32 v87, v93
	v_exp_f32_e32 v84, v94
	v_exp_f32_e32 v85, v95
	v_exp_f32_e32 v91, v97
	v_exp_f32_e32 v96, v100
	v_exp_f32_e32 v97, v101
	s_waitcnt lgkmcnt(1)
	v_mfma_f32_32x32x16_bf16 v[18:33], v[178:181], v[166:169], v[18:33]
	v_cvt_pk_bf16_f32 v166, v88, v89
	v_cvt_pk_bf16_f32 v167, v86, v87
	v_cvt_pk_bf16_f32 v168, v84, v85
	v_cvt_pk_bf16_f32 v169, v90, v91
	v_exp_f32_e32 v94, v102
	v_exp_f32_e32 v95, v103
	ds_read_b128 v[100:103], v165 offset:13376
	v_mfma_f32_32x32x16_bf16 v[34:49], v[170:173], v[166:169], v[34:49]
	v_exp_f32_e32 v92, v104
	v_exp_f32_e32 v93, v105
	ds_read_b128 v[170:173], v165 offset:17984
	ds_read_b128 v[178:181], v165 offset:13408
	v_exp_f32_e32 v104, v106
	v_exp_f32_e32 v105, v107
	v_exp_f32_e32 v106, v112
	v_exp_f32_e32 v107, v113
	s_waitcnt lgkmcnt(3)
	v_mfma_f32_32x32x16_bf16 v[18:33], v[182:185], v[166:169], v[18:33]
	v_cvt_pk_bf16_f32 v166, v98, v99
	v_cvt_pk_bf16_f32 v167, v96, v97
	v_cvt_pk_bf16_f32 v168, v94, v95
	v_cvt_pk_bf16_f32 v169, v92, v93
	ds_read_b128 v[182:185], v165 offset:18016
	v_cvt_pk_bf16_f32 v113, v106, v107
	s_waitcnt lgkmcnt(3)
	v_mfma_f32_32x32x16_bf16 v[34:49], v[100:103], v[166:169], v[34:49]
	v_exp_f32_e32 v102, v108
	v_exp_f32_e32 v103, v109
	v_exp_f32_e32 v100, v110
	v_exp_f32_e32 v101, v111
	v_cvt_pk_bf16_f32 v110, v104, v105
	v_cvt_pk_bf16_f32 v111, v102, v103
	v_lshl_add_u32 v108, v155, 1, s42
	s_waitcnt lgkmcnt(2)
	v_mfma_f32_32x32x16_bf16 v[18:33], v[170:173], v[166:169], v[18:33]
	v_cvt_pk_bf16_f32 v112, v100, v101
	v_lshl_add_u32 v109, v145, 1, v108
	s_waitcnt vmcnt(1)
	ds_write_b128 v109, v[4:7]
	s_waitcnt lgkmcnt(2)
	v_mfma_f32_32x32x16_bf16 v[34:49], v[178:181], v[110:113], v[34:49]
	s_waitcnt lgkmcnt(1)
	v_mfma_f32_32x32x16_bf16 v[18:33], v[182:185], v[110:113], v[18:33]
	s_and_saveexec_b64 s[4:5], s[0:1]
	v_add3_u32 v4, s42, v156, v154
	ds_write_b128 v4, v[138:141] offset:128
	s_or_b64 exec, exec, s[4:5]
	v_add_u32_e32 v4, v108, v161
	v_readlane_b32 s20, v252, 59
	v_add3_u32 v4, v4, v157, v158
	v_readlane_b32 s21, v252, 60
	v_add_u32_e32 v4, 0x3000, v4
	s_min_u32 s5, s37, s36
	s_mov_b64 s[10:11], -1
	s_and_b64 vcc, exec, s[20:21]
	s_waitcnt vmcnt(0)
	ds_write2_b64 v4, v[8:9], v[10:11] offset0:128 offset1:130
	s_waitcnt lgkmcnt(0)
	s_barrier
	s_cbranch_vccz .LBB0_1252
	s_lshl_b32 s4, s5, 6
	v_readlane_b32 s10, v249, 43
	s_add_i32 s4, s4, s10
	s_mov_b64 s[10:11], 0

.LBB0_1259:
	s_or_b64 exec, exec, s[10:11]
	v_add_f32_e32 v8, v152, v12
	v_add_f32_e32 v9, v153, v13
	s_ashr_i32 s5, s4, 31
	v_add_f32_e32 v8, v98, v8
	v_add_f32_e32 v9, v99, v9
	v_add3_u32 v2, s42, v159, v160
	v_add_f32_e32 v8, v82, v8
	v_add_f32_e32 v9, v83, v9
	v_xor_b32_e32 v82, 0x80000000, v164
	v_add_f32_e32 v8, v96, v8
	v_add_f32_e32 v9, v97, v9
	v_mov_b32_e32 v83, v82
	v_add_f32_e32 v8, v16, v8
	v_add_f32_e32 v9, v17, v9
	v_mov_b32_e32 v96, v82
	v_add_f32_e32 v8, v94, v8
	v_add_f32_e32 v9, v95, v9
	v_mov_b32_e32 v94, v82
	v_add_f32_e32 v8, v14, v8
	v_add_f32_e32 v9, v15, v9
	ds_read_b128 v[14:17], v2 offset:6656
	v_add_f32_e32 v8, v92, v8
	v_add_f32_e32 v9, v93, v9
	v_mov_b32_e32 v92, v82
	v_add_f32_e32 v8, v88, v8
	v_add_f32_e32 v9, v89, v9
	v_mov_b32_e32 v88, v82
	v_add_f32_e32 v8, v104, v8
	v_add_f32_e32 v9, v105, v9
	v_mov_b32_e32 v89, v82
	v_add_f32_e32 v8, v86, v8
	v_add_f32_e32 v9, v87, v9
	v_mov_b32_e32 v86, v82
	v_add_f32_e32 v8, v102, v8
	v_add_f32_e32 v9, v103, v9
	v_mov_b32_e32 v87, v82
	v_add_f32_e32 v8, v84, v8
	v_add_f32_e32 v9, v85, v9
	v_mov_b32_e32 v84, v82
	v_add_f32_e32 v8, v100, v8
	v_add_f32_e32 v9, v101, v9
	v_mov_b32_e32 v85, v82
	v_add_f32_e32 v8, v90, v8
	v_add_f32_e32 v9, v91, v9
	v_mov_b32_e32 v90, v82
	v_add_f32_e32 v12, v106, v8
	v_add_f32_e32 v13, v107, v9
	v_lshl_add_u64 v[8:9], s[4:5], 1, v[148:149]
	global_load_dwordx4 v[8:11], v[8:9], off
	v_mov_b32_e32 v91, v82
	v_mov_b32_e32 v93, v82
	v_mov_b32_e32 v95, v82
	v_mov_b32_e32 v97, v82
	v_max_i32_e32 v152, v66, v50
	v_max3_i32 v152, v152, v67, v51
	s_waitcnt lgkmcnt(0)
	v_mfma_f32_32x32x16_bf16 v[98:113], v[14:17], v[114:117], v[82:97]
	ds_read_b128 v[14:17], v2
	ds_read_b128 v[166:169], v2 offset:32
	ds_read_b128 v[170:173], v2 offset:6688
	ds_read_b128 v[186:189], v2 offset:64
	ds_read_b128 v[190:193], v2 offset:96
	ds_read_b128 v[194:197], v2 offset:128
	ds_read_b128 v[198:201], v2 offset:160
	ds_read_b128 v[202:205], v2 offset:6720
	ds_read_b128 v[206:209], v2 offset:6752
	ds_read_b128 v[226:229], v2 offset:6784
	ds_read_b128 v[230:233], v2 offset:6816
	v_max3_i32 v152, v152, v68, v52
	v_max3_i32 v152, v152, v69, v53
	v_max3_i32 v152, v152, v70, v54
	v_max3_i32 v152, v152, v71, v55
	v_max3_i32 v152, v152, v72, v56
	v_max3_i32 v152, v152, v73, v57
	s_waitcnt lgkmcnt(10)
	v_mfma_f32_32x32x16_bf16 v[82:97], v[14:17], v[114:117], v[82:97]
	v_max3_i32 v152, v152, v74, v58
	v_max3_i32 v152, v152, v75, v59
	v_max3_i32 v152, v152, v76, v60
	v_max3_i32 v152, v152, v77, v61
	v_max3_i32 v152, v152, v78, v62
	v_max3_i32 v152, v152, v79, v63
	v_max3_i32 v152, v152, v80, v64
	s_waitcnt lgkmcnt(8)
	v_mfma_f32_32x32x16_bf16 v[98:113], v[170:173], v[118:121], v[98:113]
	v_max3_i32 v152, v152, v81, v65
	v_mov_b32_e32 v14, v152
	s_nop 1
	v_permlane32_swap_b32_e32 v152, v14
	v_max_i32_e32 v14, v152, v14
	v_cmp_lt_f32_e32 vcc, s29, v14
	v_mfma_f32_32x32x16_bf16 v[82:97], v[166:169], v[118:121], v[82:97]
	s_cbranch_vccz .LBB0_1261
	v_add_f32_e32 v14, v164, v14
	v_cndmask_b32_e32 v15, v164, v14, vcc
	v_sub_f32_e32 v16, v15, v164
	v_exp_f32_e64 v14, -v16
	v_sub_f32_e32 v81, v81, v16
	v_sub_f32_e32 v80, v80, v16
	v_sub_f32_e32 v79, v79, v16
	v_pk_mul_f32 v[48:49], v[48:49], v[14:15] op_sel_hi:[1,0]
	v_pk_mul_f32 v[46:47], v[46:47], v[14:15] op_sel_hi:[1,0]
	v_pk_mul_f32 v[44:45], v[44:45], v[14:15] op_sel_hi:[1,0]
	v_pk_mul_f32 v[42:43], v[42:43], v[14:15] op_sel_hi:[1,0]
	v_pk_mul_f32 v[40:41], v[40:41], v[14:15] op_sel_hi:[1,0]
	v_pk_mul_f32 v[38:39], v[38:39], v[14:15] op_sel_hi:[1,0]
	v_pk_mul_f32 v[36:37], v[36:37], v[14:15] op_sel_hi:[1,0]
	v_pk_mul_f32 v[34:35], v[34:35], v[14:15] op_sel_hi:[1,0]
	v_pk_mul_f32 v[32:33], v[32:33], v[14:15] op_sel_hi:[1,0]
	v_pk_mul_f32 v[30:31], v[30:31], v[14:15] op_sel_hi:[1,0]
	v_pk_mul_f32 v[28:29], v[28:29], v[14:15] op_sel_hi:[1,0]
	v_pk_mul_f32 v[26:27], v[26:27], v[14:15] op_sel_hi:[1,0]
	v_pk_mul_f32 v[24:25], v[24:25], v[14:15] op_sel_hi:[1,0]
	v_pk_mul_f32 v[22:23], v[22:23], v[14:15] op_sel_hi:[1,0]
	v_pk_mul_f32 v[20:21], v[20:21], v[14:15] op_sel_hi:[1,0]
	v_pk_mul_f32 v[18:19], v[18:19], v[14:15] op_sel_hi:[1,0]
	v_sub_f32_e32 v78, v78, v16
	v_sub_f32_e32 v77, v77, v16
	v_sub_f32_e32 v76, v76, v16
	v_sub_f32_e32 v75, v75, v16
	v_sub_f32_e32 v74, v74, v16
	v_sub_f32_e32 v73, v73, v16
	v_sub_f32_e32 v72, v72, v16
	v_sub_f32_e32 v71, v71, v16
	v_sub_f32_e32 v70, v70, v16
	v_sub_f32_e32 v69, v69, v16
	v_sub_f32_e32 v68, v68, v16
	v_sub_f32_e32 v67, v67, v16
	v_sub_f32_e32 v66, v66, v16
	v_sub_f32_e32 v65, v65, v16
	v_sub_f32_e32 v64, v64, v16
	v_sub_f32_e32 v63, v63, v16
	v_sub_f32_e32 v62, v62, v16
	v_sub_f32_e32 v61, v61, v16
	v_sub_f32_e32 v60, v60, v16
	v_sub_f32_e32 v59, v59, v16
	v_sub_f32_e32 v58, v58, v16
	v_sub_f32_e32 v57, v57, v16
	v_sub_f32_e32 v56, v56, v16
	v_sub_f32_e32 v55, v55, v16
	v_sub_f32_e32 v54, v54, v16
	v_sub_f32_e32 v53, v53, v16
	v_sub_f32_e32 v52, v52, v16
	v_sub_f32_e32 v51, v51, v16
	v_sub_f32_e32 v50, v50, v16
	v_sub_f32_e32 v97, v97, v16
	v_sub_f32_e32 v96, v96, v16
	v_sub_f32_e32 v95, v95, v16
	v_sub_f32_e32 v94, v94, v16
	v_sub_f32_e32 v93, v93, v16
	v_sub_f32_e32 v92, v92, v16
	v_sub_f32_e32 v91, v91, v16
	v_sub_f32_e32 v90, v90, v16
	v_sub_f32_e32 v89, v89, v16
	v_sub_f32_e32 v88, v88, v16
	v_sub_f32_e32 v87, v87, v16
	v_sub_f32_e32 v86, v86, v16
	v_sub_f32_e32 v85, v85, v16
	v_sub_f32_e32 v84, v84, v16
	v_sub_f32_e32 v83, v83, v16
	v_sub_f32_e32 v82, v82, v16
	v_sub_f32_e32 v113, v113, v16
	v_sub_f32_e32 v112, v112, v16
	v_sub_f32_e32 v111, v111, v16
	v_sub_f32_e32 v110, v110, v16
	v_sub_f32_e32 v109, v109, v16
	v_sub_f32_e32 v108, v108, v16
	v_sub_f32_e32 v107, v107, v16
	v_sub_f32_e32 v106, v106, v16
	v_sub_f32_e32 v105, v105, v16
	v_sub_f32_e32 v104, v104, v16
	v_sub_f32_e32 v103, v103, v16
	v_sub_f32_e32 v102, v102, v16
	v_sub_f32_e32 v101, v101, v16
	v_sub_f32_e32 v100, v100, v16
	v_sub_f32_e32 v99, v99, v16
	v_sub_f32_e32 v98, v98, v16
	v_pk_mul_f32 v[12:13], v[12:13], v[14:15] op_sel_hi:[1,0]
	v_mov_b32_e32 v164, v15
.LBB0_1261:
	v_add3_u32 v152, s40, v162, v160
	v_exp_f32_e32 v66, v66
	v_exp_f32_e32 v67, v67
	s_waitcnt lgkmcnt(7)
	v_mfma_f32_32x32x16_bf16 v[82:97], v[186:189], v[122:125], v[82:97]
	v_exp_f32_e32 v74, v74
	v_exp_f32_e32 v75, v75
	v_exp_f32_e32 v52, v52
	v_exp_f32_e32 v53, v53
	s_addk_i32 s41, 0x5800
	s_cmp_lg_u32 s39, 2
	s_cselect_b32 s4, s41, 0
	s_waitcnt lgkmcnt(6)
	v_mfma_f32_32x32x16_bf16 v[82:97], v[190:193], v[126:129], v[82:97]
	s_add_i32 s10, s4, 0
	s_waitcnt lgkmcnt(5)
	v_mfma_f32_32x32x16_bf16 v[82:97], v[194:197], v[130:133], v[82:97]
	s_waitcnt lgkmcnt(4)
	v_mfma_f32_32x32x16_bf16 v[82:97], v[198:201], v[134:137], v[82:97]
	ds_read_b128 v[170:173], v152 offset:13312
	ds_read_b128 v[178:181], v152 offset:13344
	ds_read_b128 v[182:185], v152 offset:17952
	s_waitcnt lgkmcnt(6)
	v_mfma_f32_32x32x16_bf16 v[98:113], v[202:205], v[122:125], v[98:113]
	s_waitcnt lgkmcnt(5)
	v_mfma_f32_32x32x16_bf16 v[98:113], v[206:209], v[126:129], v[98:113]
	v_lshl_add_u32 v2, v155, 1, s10
	s_waitcnt lgkmcnt(4)
	v_mfma_f32_32x32x16_bf16 v[98:113], v[226:229], v[130:133], v[98:113]
	v_exp_f32_e32 v16, v68
	v_exp_f32_e32 v17, v69
	v_exp_f32_e32 v14, v70
	v_exp_f32_e32 v15, v71
	v_exp_f32_e32 v68, v72
	v_exp_f32_e32 v69, v73
	v_exp_f32_e32 v72, v76
	s_waitcnt lgkmcnt(0)
	v_mfma_f32_32x32x16_bf16 v[98:113], v[230:233], v[134:137], v[98:113]
	v_cvt_pk_bf16_f32 v166, v66, v67
	v_cvt_pk_bf16_f32 v167, v16, v17
	v_cvt_pk_bf16_f32 v168, v14, v15
	v_cvt_pk_bf16_f32 v169, v68, v69
	v_exp_f32_e32 v73, v77
	v_exp_f32_e32 v70, v78
	v_exp_f32_e32 v71, v79
	v_mfma_f32_32x32x16_bf16 v[34:49], v[170:173], v[166:169], v[34:49]
	ds_read_b128 v[170:173], v152 offset:17920
	v_exp_f32_e32 v76, v80
	v_exp_f32_e32 v77, v81
	v_exp_f32_e32 v78, v50
	v_exp_f32_e32 v79, v51
	v_exp_f32_e32 v50, v54
	v_exp_f32_e32 v51, v55
	s_waitcnt lgkmcnt(0)
	v_mfma_f32_32x32x16_bf16 v[18:33], v[170:173], v[166:169], v[18:33]
	v_cvt_pk_bf16_f32 v166, v74, v75
	v_cvt_pk_bf16_f32 v167, v72, v73
	v_cvt_pk_bf16_f32 v168, v70, v71
	v_cvt_pk_bf16_f32 v169, v76, v77
	ds_read_b128 v[170:173], v152 offset:13376
	v_exp_f32_e32 v54, v56
	v_exp_f32_e32 v55, v57
	v_mfma_f32_32x32x16_bf16 v[34:49], v[178:181], v[166:169], v[34:49]
	ds_read_b128 v[178:181], v152 offset:13408
	v_exp_f32_e32 v80, v58
	v_exp_f32_e32 v81, v59
	v_exp_f32_e32 v58, v60
	v_exp_f32_e32 v59, v61
	v_exp_f32_e32 v56, v62
	v_exp_f32_e32 v57, v63
	v_mfma_f32_32x32x16_bf16 v[18:33], v[182:185], v[166:169], v[18:33]
	v_cvt_pk_bf16_f32 v166, v78, v79
	v_cvt_pk_bf16_f32 v167, v52, v53
	v_cvt_pk_bf16_f32 v168, v50, v51
	v_cvt_pk_bf16_f32 v169, v54, v55
	ds_read_b128 v[182:185], v152 offset:18016
	v_exp_f32_e32 v60, v64
	v_exp_f32_e32 v61, v65
	s_waitcnt lgkmcnt(2)
	v_mfma_f32_32x32x16_bf16 v[34:49], v[170:173], v[166:169], v[34:49]
	ds_read_b128 v[170:173], v152 offset:17984
	v_cvt_pk_bf16_f32 v62, v80, v81
	v_cvt_pk_bf16_f32 v63, v58, v59
	v_cvt_pk_bf16_f32 v64, v56, v57
	v_cvt_pk_bf16_f32 v65, v60, v61
	v_lshl_add_u32 v152, v145, 1, v2
	s_waitcnt vmcnt(1)
	ds_write_b128 v152, v[4:7]
	s_waitcnt lgkmcnt(1)
	v_mfma_f32_32x32x16_bf16 v[18:33], v[170:173], v[166:169], v[18:33]
	v_mfma_f32_32x32x16_bf16 v[34:49], v[178:181], v[62:65], v[34:49]
	v_mfma_f32_32x32x16_bf16 v[18:33], v[182:185], v[62:65], v[18:33]
	s_and_saveexec_b64 s[4:5], s[0:1]
	s_cbranch_execz .LBB0_1236
	v_add3_u32 v4, s10, v156, v154
	ds_write_b128 v4, v[138:141] offset:128
	s_branch .LBB0_1236

.LBB0_1376:
	s_or_b64 exec, exec, s[4:5]
	v_cvt_f32_u32_e32 v6, v4
	s_waitcnt vmcnt(0)
	v_readfirstlane_b32 s4, v5
	v_sub_u32_e32 v5, 0, v4
	v_rcp_iflag_f32_e32 v6, v6
	v_add_u32_e32 v7, s4, v1
	v_mul_f32_e32 v6, 0x4f7ffffe, v6
	v_cvt_u32_f32_e32 v6, v6
	v_mul_lo_u32 v1, v5, v6
	v_mul_hi_u32 v1, v6, v1
	v_add_u32_e32 v1, v6, v1
	v_mul_hi_u32 v1, v7, v1
	v_mul_lo_u32 v5, v1, v4
	v_sub_u32_e32 v5, v7, v5
	v_add_u32_e32 v6, 1, v1
	v_cmp_ge_u32_e32 vcc, v5, v4
	s_nop 1
	v_cndmask_b32_e32 v1, v1, v6, vcc
	v_sub_u32_e32 v6, v5, v4
	v_cndmask_b32_e32 v5, v5, v6, vcc
	v_add_u32_e32 v6, 1, v1
	v_cmp_ge_u32_e32 vcc, v5, v4
	v_add_u32_e32 v5, 1, v7
	s_nop 0
	v_cndmask_b32_e32 v1, v1, v6, vcc
	v_mul_lo_u32 v6, v4, v1
	v_add_u32_e32 v4, v6, v4
	v_cmp_ne_u32_e32 vcc, v5, v4
	s_and_saveexec_b64 s[4:5], vcc
	s_xor_b64 s[4:5], exec, s[4:5]
	s_cbranch_execz .LBB0_1390
	v_readlane_b32 s10, v250, 62
	v_readlane_b32 s11, v250, 63
	s_waitcnt lgkmcnt(0)
	v_add_u32_e32 v1, 1, v1
	v_mul_lo_u32 v1, v1, v2
	s_nop 3
	global_load_dword v2, v3, s[10:11] sc1
	s_waitcnt vmcnt(0)
	v_cmp_lt_u32_e32 vcc, v2, v1
	s_and_saveexec_b64 s[36:37], vcc
	s_cbranch_execz .LBB0_1389
	s_mov_b32 s42, 1
	s_mov_b64 s[38:39], 0
	s_branch .LBB0_1380

.LBB0_1382:
	v_readlane_b32 s10, v250, 62
	v_readlane_b32 s11, v250, 63
	s_add_i32 s42, s42, 1
	s_mov_b64 s[44:45], -1
	s_nop 2
	global_load_dword v2, v3, s[10:11] sc1
	s_waitcnt vmcnt(0)
	v_cmp_ge_u32_e32 vcc, v2, v1
	s_orn2_b64 s[10:11], vcc, exec
	s_branch .LBB0_1379

.LBB0_1393:
	s_or_b64 exec, exec, s[10:11]
	s_waitcnt vmcnt(0)
	v_readfirstlane_b32 s4, v4
	v_sub_u32_e32 v5, 0, v2
	s_mov_b64 s[10:11], 0
	v_add_u32_e32 v4, s4, v1
	v_cvt_f32_u32_e32 v1, v2
	v_readlane_b32 s4, v251, 0
	v_readlane_b32 s5, v251, 1
	v_rcp_iflag_f32_e32 v1, v1
	s_nop 0
	v_mul_f32_e32 v1, 0x4f7ffffe, v1
	v_cvt_u32_f32_e32 v1, v1
	v_mul_lo_u32 v5, v5, v1
	v_mul_hi_u32 v5, v1, v5
	v_add_u32_e32 v1, v1, v5
	v_mul_hi_u32 v1, v4, v1
	v_mul_lo_u32 v5, v1, v2
	v_sub_u32_e32 v5, v4, v5
	v_cmp_ge_u32_e32 vcc, v5, v2
	v_add_u32_e32 v6, 1, v1
	v_add_u32_e32 v4, 1, v4
	v_cndmask_b32_e32 v1, v1, v6, vcc
	v_sub_u32_e32 v6, v5, v2
	v_cndmask_b32_e32 v5, v5, v6, vcc
	v_cmp_ge_u32_e32 vcc, v5, v2
	v_add_u32_e32 v5, 1, v1
	s_nop 0
	v_cndmask_b32_e32 v1, v1, v5, vcc
	v_mul_lo_u32 v5, v2, v1
	v_add_u32_e32 v2, v5, v2
	v_cmp_ne_u32_e32 vcc, v4, v2
	v_mov_b32_e32 v1, v2
	v_mov_b64_e32 v[4:5], s[4:5]
	s_and_saveexec_b64 s[4:5], vcc
	s_cbranch_execz .LBB0_1405
	v_readlane_b32 s10, v250, 62
	v_readlane_b32 s11, v250, 63
	s_nop 4
	global_load_dword v2, v3, s[10:11] sc1
	s_mov_b64 s[10:11], 0
	s_waitcnt vmcnt(0)
	v_cmp_lt_u32_e32 vcc, v2, v1
	s_and_saveexec_b64 s[36:37], vcc
	s_cbranch_execz .LBB0_1404
	s_mov_b32 s42, 1
	s_mov_b64 s[38:39], 0
	s_branch .LBB0_1397

.LBB0_1407:
	s_or_b64 exec, exec, s[4:5]
	s_mov_b64 s[4:5], exec
	v_mbcnt_lo_u32_b32 v1, s4, 0
	v_mbcnt_hi_u32_b32 v1, s5, v1
	v_cmp_eq_u32_e32 vcc, 0, v1
	s_waitcnt vmcnt(0)
	buffer_inv sc1
	s_and_saveexec_b64 s[10:11], vcc
	s_cbranch_execz .LBB0_1409
	s_bcnt1_i32_b64 s4, s[4:5]
	v_mov_b32_e32 v1, s4
	v_readlane_b32 s4, v250, 60
	v_readlane_b32 s5, v250, 61
	s_nop 4
.LBB0_1409:
	s_or_b64 exec, exec, s[10:11]
	s_waitcnt vmcnt(0)

.LBB0_1495:
	s_or_b64 exec, exec, s[4:5]
	s_mov_b64 s[4:5], exec
	v_mbcnt_lo_u32_b32 v1, s4, 0
	v_mbcnt_hi_u32_b32 v1, s5, v1
	v_cmp_eq_u32_e32 vcc, 0, v1
	s_waitcnt vmcnt(0)
	buffer_inv sc1
	s_and_saveexec_b64 s[10:11], vcc
	s_cbranch_execz .LBB0_1497
	s_bcnt1_i32_b64 s4, s[4:5]
	v_mov_b32_e32 v1, s4
	v_readlane_b32 s4, v250, 60
	v_readlane_b32 s5, v250, 61
	s_nop 4
.LBB0_1497:
	s_or_b64 exec, exec, s[10:11]
	s_waitcnt vmcnt(0)

.LBB0_1611:
	s_or_b64 exec, exec, s[4:5]
	v_cvt_f32_u32_e32 v6, v4
	s_waitcnt vmcnt(0)
	v_readfirstlane_b32 s4, v5
	v_sub_u32_e32 v5, 0, v4
	v_rcp_iflag_f32_e32 v6, v6
	v_add_u32_e32 v7, s4, v1
	v_mul_f32_e32 v6, 0x4f7ffffe, v6
	v_cvt_u32_f32_e32 v6, v6
	v_mul_lo_u32 v1, v5, v6
	v_mul_hi_u32 v1, v6, v1
	v_add_u32_e32 v1, v6, v1
	v_mul_hi_u32 v1, v7, v1
	v_mul_lo_u32 v5, v1, v4
	v_sub_u32_e32 v5, v7, v5
	v_add_u32_e32 v6, 1, v1
	v_cmp_ge_u32_e32 vcc, v5, v4
	s_nop 1
	v_cndmask_b32_e32 v1, v1, v6, vcc
	v_sub_u32_e32 v6, v5, v4
	v_cndmask_b32_e32 v5, v5, v6, vcc
	v_add_u32_e32 v6, 1, v1
	v_cmp_ge_u32_e32 vcc, v5, v4
	v_add_u32_e32 v5, 1, v7
	s_nop 0
	v_cndmask_b32_e32 v1, v1, v6, vcc
	v_mul_lo_u32 v6, v4, v1
	v_add_u32_e32 v4, v6, v4
	v_cmp_ne_u32_e32 vcc, v5, v4
	s_and_saveexec_b64 s[4:5], vcc
	s_xor_b64 s[4:5], exec, s[4:5]
	s_cbranch_execz .LBB0_1625
	v_readlane_b32 s10, v250, 62
	v_readlane_b32 s11, v250, 63
	s_waitcnt lgkmcnt(0)
	v_add_u32_e32 v1, 1, v1
	v_mul_lo_u32 v1, v1, v2
	s_nop 3
	global_load_dword v2, v3, s[10:11] sc1
	s_waitcnt vmcnt(0)
	v_cmp_lt_u32_e32 vcc, v2, v1
	s_and_saveexec_b64 s[14:15], vcc
	s_cbranch_execz .LBB0_1624
	s_mov_b32 s42, 1
	s_mov_b64 s[36:37], 0
	s_branch .LBB0_1615

.LBB0_1617:
	v_readlane_b32 s10, v250, 62
	v_readlane_b32 s11, v250, 63
	s_add_i32 s42, s42, 1
	s_mov_b64 s[40:41], -1
	s_nop 2
	global_load_dword v2, v3, s[10:11] sc1
	s_waitcnt vmcnt(0)
	v_cmp_ge_u32_e32 vcc, v2, v1
	s_orn2_b64 s[10:11], vcc, exec
	s_branch .LBB0_1614

.LBB0_1628:
	s_or_b64 exec, exec, s[10:11]
	s_waitcnt vmcnt(0)
	v_readfirstlane_b32 s4, v4
	v_sub_u32_e32 v5, 0, v2
	s_mov_b64 s[10:11], 0
	v_add_u32_e32 v4, s4, v1
	v_cvt_f32_u32_e32 v1, v2
	v_readlane_b32 s4, v251, 0
	v_readlane_b32 s5, v251, 1
	v_rcp_iflag_f32_e32 v1, v1
	s_nop 0
	v_mul_f32_e32 v1, 0x4f7ffffe, v1
	v_cvt_u32_f32_e32 v1, v1
	v_mul_lo_u32 v5, v5, v1
	v_mul_hi_u32 v5, v1, v5
	v_add_u32_e32 v1, v1, v5
	v_mul_hi_u32 v1, v4, v1
	v_mul_lo_u32 v5, v1, v2
	v_sub_u32_e32 v5, v4, v5
	v_cmp_ge_u32_e32 vcc, v5, v2
	v_add_u32_e32 v6, 1, v1
	v_add_u32_e32 v4, 1, v4
	v_cndmask_b32_e32 v1, v1, v6, vcc
	v_sub_u32_e32 v6, v5, v2
	v_cndmask_b32_e32 v5, v5, v6, vcc
	v_cmp_ge_u32_e32 vcc, v5, v2
	v_add_u32_e32 v5, 1, v1
	s_nop 0
	v_cndmask_b32_e32 v1, v1, v5, vcc
	v_mul_lo_u32 v5, v2, v1
	v_add_u32_e32 v2, v5, v2
	v_cmp_ne_u32_e32 vcc, v4, v2
	v_mov_b32_e32 v1, v2
	v_mov_b64_e32 v[4:5], s[4:5]
	s_and_saveexec_b64 s[4:5], vcc
	s_cbranch_execz .LBB0_1640
	v_readlane_b32 s10, v250, 62
	v_readlane_b32 s11, v250, 63
	s_nop 4
	global_load_dword v2, v3, s[10:11] sc1
	s_mov_b64 s[10:11], 0
	s_waitcnt vmcnt(0)
	v_cmp_lt_u32_e32 vcc, v2, v1
	s_and_saveexec_b64 s[14:15], vcc
	s_cbranch_execz .LBB0_1639
	s_mov_b32 s42, 1
	s_mov_b64 s[36:37], 0
	s_branch .LBB0_1632

.LBB0_1642:
	s_or_b64 exec, exec, s[4:5]
	s_mov_b64 s[4:5], exec
	v_mbcnt_lo_u32_b32 v1, s4, 0
	v_mbcnt_hi_u32_b32 v1, s5, v1
	v_cmp_eq_u32_e32 vcc, 0, v1
	s_waitcnt vmcnt(0)
	buffer_inv sc1
	s_and_saveexec_b64 s[10:11], vcc
	s_cbranch_execz .LBB0_1644
	s_bcnt1_i32_b64 s4, s[4:5]
	v_mov_b32_e32 v1, s4
	v_readlane_b32 s4, v250, 60
	v_readlane_b32 s5, v250, 61
	s_nop 4
.LBB0_1644:
	s_or_b64 exec, exec, s[10:11]
	s_waitcnt vmcnt(0)

.LBB0_1755:
	s_or_b64 exec, exec, s[4:5]
	s_mov_b64 s[4:5], exec
	v_mbcnt_lo_u32_b32 v1, s4, 0
	v_mbcnt_hi_u32_b32 v1, s5, v1
	v_cmp_eq_u32_e32 vcc, 0, v1
	s_waitcnt vmcnt(0)
	buffer_inv sc1
	s_and_saveexec_b64 s[10:11], vcc
	s_cbranch_execz .LBB0_1757
	s_bcnt1_i32_b64 s4, s[4:5]
	v_mov_b32_e32 v1, s4
	v_readlane_b32 s4, v250, 60
	v_readlane_b32 s5, v250, 61
	s_nop 4
.LBB0_1757:
	s_or_b64 exec, exec, s[10:11]
	s_waitcnt vmcnt(0)

.LBB0_1869:
	s_or_b64 exec, exec, s[4:5]
	s_mov_b64 s[4:5], exec
	v_mbcnt_lo_u32_b32 v1, s4, 0
	v_mbcnt_hi_u32_b32 v1, s5, v1
	v_cmp_eq_u32_e32 vcc, 0, v1
	s_waitcnt vmcnt(0)
	buffer_inv sc1
	s_and_saveexec_b64 s[10:11], vcc
	s_cbranch_execz .LBB0_1871
	s_bcnt1_i32_b64 s4, s[4:5]
	v_mov_b32_e32 v1, s4
	v_readlane_b32 s4, v250, 60
	v_readlane_b32 s5, v250, 61
	s_nop 4
.LBB0_1871:
	s_or_b64 exec, exec, s[10:11]
	s_waitcnt vmcnt(0)

.LBB0_2005:
	s_or_b64 exec, exec, s[4:5]
	s_mov_b64 s[4:5], exec
	v_mbcnt_lo_u32_b32 v1, s4, 0
	v_mbcnt_hi_u32_b32 v1, s5, v1
	v_cmp_eq_u32_e32 vcc, 0, v1
	s_waitcnt vmcnt(0)
	buffer_inv sc1
	s_and_saveexec_b64 s[10:11], vcc
	s_cbranch_execz .LBB0_2007
	s_bcnt1_i32_b64 s4, s[4:5]
	v_mov_b32_e32 v1, s4
	v_readlane_b32 s4, v250, 60
	v_readlane_b32 s5, v250, 61
	s_nop 4
.LBB0_2007:
	s_or_b64 exec, exec, s[10:11]
	s_waitcnt vmcnt(0)

.LBB0_2136:
	s_or_b64 exec, exec, s[4:5]
	v_cvt_f32_u32_e32 v6, v4
	s_waitcnt vmcnt(0)
	v_readfirstlane_b32 s4, v5
	v_sub_u32_e32 v5, 0, v4
	v_rcp_iflag_f32_e32 v6, v6
	v_add_u32_e32 v7, s4, v1
	v_mul_f32_e32 v6, 0x4f7ffffe, v6
	v_cvt_u32_f32_e32 v6, v6
	v_mul_lo_u32 v1, v5, v6
	v_mul_hi_u32 v1, v6, v1
	v_add_u32_e32 v1, v6, v1
	v_mul_hi_u32 v1, v7, v1
	v_mul_lo_u32 v5, v1, v4
	v_sub_u32_e32 v5, v7, v5
	v_add_u32_e32 v6, 1, v1
	v_cmp_ge_u32_e32 vcc, v5, v4
	s_nop 1
	v_cndmask_b32_e32 v1, v1, v6, vcc
	v_sub_u32_e32 v6, v5, v4
	v_cndmask_b32_e32 v5, v5, v6, vcc
	v_add_u32_e32 v6, 1, v1
	v_cmp_ge_u32_e32 vcc, v5, v4
	v_add_u32_e32 v5, 1, v7
	s_nop 0
	v_cndmask_b32_e32 v1, v1, v6, vcc
	v_mul_lo_u32 v6, v4, v1
	v_add_u32_e32 v4, v6, v4
	v_cmp_ne_u32_e32 vcc, v5, v4
	s_and_saveexec_b64 s[4:5], vcc
	s_xor_b64 s[4:5], exec, s[4:5]
	s_cbranch_execz .LBB0_2150
	v_readlane_b32 s10, v250, 62
	v_readlane_b32 s11, v250, 63
	s_waitcnt lgkmcnt(0)
	v_add_u32_e32 v1, 1, v1
	v_mul_lo_u32 v1, v1, v2
	s_nop 3
	global_load_dword v2, v3, s[10:11] sc1
	s_waitcnt vmcnt(0)
	v_cmp_lt_u32_e32 vcc, v2, v1
	s_and_saveexec_b64 s[14:15], vcc
	s_cbranch_execz .LBB0_2149
	s_mov_b32 s12, 1
	s_mov_b64 s[36:37], 0
	s_branch .LBB0_2140

.LBB0_2142:
	v_readlane_b32 s10, v250, 62
	v_readlane_b32 s11, v250, 63
	s_add_i32 s12, s12, 1
	s_mov_b64 s[40:41], -1
	s_nop 2
	global_load_dword v2, v3, s[10:11] sc1
	s_waitcnt vmcnt(0)
	v_cmp_ge_u32_e32 vcc, v2, v1
	s_orn2_b64 s[10:11], vcc, exec
	s_branch .LBB0_2139

.LBB0_2153:
	s_or_b64 exec, exec, s[10:11]
	s_waitcnt vmcnt(0)
	v_readfirstlane_b32 s4, v4
	v_sub_u32_e32 v5, 0, v2
	s_mov_b64 s[10:11], 0
	v_add_u32_e32 v4, s4, v1
	v_cvt_f32_u32_e32 v1, v2
	v_readlane_b32 s4, v251, 0
	v_readlane_b32 s5, v251, 1
	v_rcp_iflag_f32_e32 v1, v1
	s_nop 0
	v_mul_f32_e32 v1, 0x4f7ffffe, v1
	v_cvt_u32_f32_e32 v1, v1
	v_mul_lo_u32 v5, v5, v1
	v_mul_hi_u32 v5, v1, v5
	v_add_u32_e32 v1, v1, v5
	v_mul_hi_u32 v1, v4, v1
	v_mul_lo_u32 v5, v1, v2
	v_sub_u32_e32 v5, v4, v5
	v_cmp_ge_u32_e32 vcc, v5, v2
	v_add_u32_e32 v6, 1, v1
	v_add_u32_e32 v4, 1, v4
	v_cndmask_b32_e32 v1, v1, v6, vcc
	v_sub_u32_e32 v6, v5, v2
	v_cndmask_b32_e32 v5, v5, v6, vcc
	v_cmp_ge_u32_e32 vcc, v5, v2
	v_add_u32_e32 v5, 1, v1
	s_nop 0
	v_cndmask_b32_e32 v1, v1, v5, vcc
	v_mul_lo_u32 v5, v2, v1
	v_add_u32_e32 v2, v5, v2
	v_cmp_ne_u32_e32 vcc, v4, v2
	v_mov_b32_e32 v1, v2
	v_mov_b64_e32 v[4:5], s[4:5]
	s_and_saveexec_b64 s[4:5], vcc
	s_cbranch_execz .LBB0_2165
	v_readlane_b32 s10, v250, 62
	v_readlane_b32 s11, v250, 63
	s_nop 4
	global_load_dword v2, v3, s[10:11] sc1
	s_mov_b64 s[10:11], 0
	s_waitcnt vmcnt(0)
	v_cmp_lt_u32_e32 vcc, v2, v1
	s_and_saveexec_b64 s[14:15], vcc
	s_cbranch_execz .LBB0_2164
	s_mov_b32 s12, 1
	s_mov_b64 s[36:37], 0
	s_branch .LBB0_2157

.LBB0_2168:
	s_bcnt1_i32_b64 s4, s[4:5]
	v_mov_b32_e32 v1, s4
	v_readlane_b32 s4, v250, 60
	v_readlane_b32 s5, v250, 61
	s_nop 4
	s_getpc_b64 s[98:99]
